# moe2 epilogue: next unit's per-row gates loaded during the current epilogue (no round trip at epilogue start)
# speedup vs baseline: 1.0052x; 1.0052x over previous
.LBB0_1272:
	s_add_u32 s44, s12, 0x44734800
	s_addc_u32 s45, s13, 0
	s_add_u32 s46, s10, 0x2c918800
	s_addc_u32 s47, s11, 0
	s_lshl_b32 s10, s37, 5
	s_and_b32 s39, s10, 0x60
	s_add_i32 m0, s21, 0x18000
	v_lshl_add_u64 v[6:7], v[6:7], 0, s[8:9]
	s_lshl_b32 s38, s36, 13
	s_lshl_b32 s37, s39, 7
	s_waitcnt vmcnt(2)
	s_barrier
	global_load_lds_dwordx4 v[6:7], off
	v_lshl_add_u64 v[4:5], v[4:5], 0, s[8:9]
	s_add_i32 m0, s21, 0x1a000
	s_add_i32 s12, s21, 0x8000
	s_add_i32 s13, s21, 0xa000
	global_load_lds_dwordx4 v[4:5], off
	v_lshl_add_u64 v[0:1], v[0:1], 0, s[8:9]
	s_mov_b32 m0, s12
	s_add_u32 s10, s4, 0x58080
	global_load_lds_dwordx4 v[0:1], off
	v_lshl_add_u64 v[0:1], v[2:3], 0, s[8:9]
	s_mov_b32 m0, s13
	s_addc_u32 s11, s5, 0
	global_load_lds_dwordx4 v[0:1], off
	s_add_i32 m0, s21, 0x1c000
	v_lshl_add_u64 v[0:1], s[10:11], 0, v[128:129]
	global_load_lds_dwordx4 v[0:1], off
	v_lshl_add_u64 v[0:1], s[10:11], 0, v[130:131]
	s_add_i32 m0, s21, 0x1e000
	s_cmpk_lt_u32 s35, 0x100
	global_load_lds_dwordx4 v[0:1], off
	v_lshrrev_b32_e32 v0, 1, v8
	v_and_b32_e32 v0, 24, v0
	v_and_b32_e32 v1, 15, v8
	v_lshlrev_b32_e32 v2, 1, v0
	v_lshl_or_b32 v138, s36, 6, v1
	v_lshl_or_b32 v1, v1, 6, v2
	v_lshlrev_b32_e32 v2, 2, v8
	s_cselect_b64 s[48:49], -1, 0
	s_and_b64 s[10:11], s[6:7], exec
	v_and_b32_e32 v2, 32, v2
	s_movk_i32 s10, 0x480
	v_bitop3_b32 v139, v1, s37, v2 bitop3:0xde
	s_cselect_b32 s35, 0x400, s10
	s_ashr_i32 s36, s19, 3
	s_ashr_i32 s37, s18, 3
	s_and_b64 s[6:7], s[6:7], exec
	s_movk_i32 s6, 0x80
	s_movk_i32 s10, 0x580
	v_bitop3_b32 v4, v1, s38, v2 bitop3:0xde
	s_cselect_b32 s56, s6, 0x90
	s_lshl_b32 s6, s18, 1
	v_lshrrev_b32_e32 v1, 1, v13
	v_mul_lo_u32 v2, v15, s10
	s_movk_i32 s11, 0x5800
	s_and_b32 s57, s6, 14
	v_mad_u64_u32 v[2:3], s[6:7], v1, s11, v[2:3]
	v_or_b32_e32 v1, v2, v14
	v_add_lshl_u32 v144, v1, v16, 1
	v_lshrrev_b32_e32 v1, 1, v9
	v_mul_lo_u32 v2, v11, s10
	v_mad_u64_u32 v[2:3], s[6:7], v1, s11, v[2:3]
	s_waitcnt vmcnt(6)
	s_mov_b64 s[52:53], 0x58080
	v_or_b32_e32 v1, v2, v10
	v_lshl_add_u64 v[132:133], v[144:145], 0, s[52:53]
	v_add_lshl_u32 v144, v1, v12, 1
	v_or_b32_e32 v140, 16, v138
	v_or_b32_e32 v141, 32, v138
	v_or_b32_e32 v142, 48, v138
	v_lshl_add_u64 v[134:135], v[144:145], 0, s[52:53]
	s_mov_b32 s58, 0
	v_add_u32_e32 v143, 0, v4
	s_lshl_b32 s50, s39, 1
	v_lshlrev_b32_e32 v144, 1, v0
	s_barrier
	s_mov_b32 s88, 0
	s_branch .LBB0_1275

; __device__ __forceinline__ u32x4 pack8(f32x4 a, f32x4 b) { u32x4 w; w.x = pk2(a[0], a[1]); w.y = pk2(a[2], a[3]); w.z = pk2(b[0], b[1]); w.w = pk2(b[2], b[3]); return w; }
;     __device__ __forceinline__ void operator()(const f32x4 (&acc)[2][2][4][2], const Unit& u, int wr, int wc, int fr, int fq) const {
;         const int jn = u.pn & 3;
; #pragma unroll
;         for (int ai = 0; ai < 2; ++ai)
; #pragma unroll
;             for (int m = 0; m < 4; ++m) {
;                 const int row = u.pm * 256 + ai * 128 + wr * 64 + m * 16 + fr; const float gt = gate[row];
; #pragma unroll
;                 for (int bj = 0; bj < 2; ++bj) *(u32x4*)(Y + (size_t)row * D + 256 * jn + 128 * bj + 32 * wc + 8 * fq) = pack8(acc[ai][bj][m][0] * gt, acc[ai][bj][m][1] * gt);
;             }
.LBB0_1301:
	s_lshl_b32 s2, s30, 8
	v_add_u32_e32 v136, s2, v138
	s_cmp_eq_u32 s88, 1
	s_cbranch_scc1 .Lm2_have
	v_lshlrev_b32_e32 v160, 2, v136
	global_load_dword v152, v160, s[46:47]
	global_load_dword v153, v160, s[46:47] offset:64
	global_load_dword v154, v160, s[46:47] offset:128
	global_load_dword v155, v160, s[46:47] offset:192
	global_load_dword v156, v160, s[46:47] offset:512
	global_load_dword v157, v160, s[46:47] offset:576
	global_load_dword v158, v160, s[46:47] offset:640
	global_load_dword v159, v160, s[46:47] offset:704
	s_waitcnt vmcnt(0)
	s_branch .Lm2_go
.Lm2_have:
	s_waitcnt vmcnt(8)
	v_mov_b32_e32 v152, v218
	v_mov_b32_e32 v153, v219
	v_mov_b32_e32 v154, v220
	v_mov_b32_e32 v155, v221
	v_mov_b32_e32 v156, v222
	v_mov_b32_e32 v157, v223
	v_mov_b32_e32 v158, v224
	v_mov_b32_e32 v159, v225
.Lm2_go:
	s_mov_b32 s88, 0
	s_cmp_eq_u64 s[38:39], 0
	s_cbranch_scc0 .Lm2_nopf
	s_lshl_b32 s3, s60, 8
	v_add_u32_e32 v226, s3, v138
	v_lshlrev_b32_e32 v226, 2, v226
	global_load_dword v218, v226, s[46:47]
	global_load_dword v219, v226, s[46:47] offset:64
	global_load_dword v220, v226, s[46:47] offset:128
	global_load_dword v221, v226, s[46:47] offset:192
	global_load_dword v222, v226, s[46:47] offset:512
	global_load_dword v223, v226, s[46:47] offset:576
	global_load_dword v224, v226, s[46:47] offset:640
	global_load_dword v225, v226, s[46:47] offset:704
	s_mov_b32 s88, 1
.Lm2_nopf:
	v_ashrrev_i32_e32 v137, 31, v136
	v_lshl_add_u64 v[146:147], v[136:137], 2, s[46:47]
	v_lshlrev_b64 v[148:149], 11, v[136:137]
	s_lshl_b32 s3, s51, 9
	s_and_b32 s30, s3, 0x600
	s_mov_b32 s51, s31
	s_and_b64 vcc, exec, s[38:39]
	v_mov_b32_e32 v146, v152
	v_pk_mul_f32 v[124:125], v[124:125], v[146:147] op_sel_hi:[1,0]
	v_pk_mul_f32 v[150:151], v[122:123], v[146:147] op_sel_hi:[1,0]
	v_pk_mul_f32 v[122:123], v[120:121], v[146:147] op_sel_hi:[1,0]
	v_cvt_pk_bf16_f32 v120, v124, v125
	v_lshl_add_u64 v[124:125], s[44:45], 0, v[148:149]
	v_lshl_add_u64 v[124:125], v[124:125], 0, s[30:31]
	v_pk_mul_f32 v[126:127], v[126:127], v[146:147] op_sel_hi:[1,0]
	v_lshl_add_u64 v[124:125], v[124:125], 0, s[50:51]
	v_cvt_pk_bf16_f32 v121, v126, v127
	v_cvt_pk_bf16_f32 v122, v122, v123
	v_cvt_pk_bf16_f32 v123, v150, v151
	v_lshl_add_u64 v[124:125], v[124:125], 0, v[144:145]
	global_store_dwordx4 v[124:125], v[120:123], off
	v_pk_mul_f32 v[118:119], v[118:119], v[146:147] op_sel_hi:[1,0]
	v_pk_mul_f32 v[116:117], v[116:117], v[146:147] op_sel_hi:[1,0]
	v_pk_mul_f32 v[120:121], v[114:115], v[146:147] op_sel_hi:[1,0]
	v_pk_mul_f32 v[114:115], v[112:113], v[146:147] op_sel_hi:[1,0]
	v_cvt_pk_bf16_f32 v112, v116, v117
	v_cvt_pk_bf16_f32 v113, v118, v119
	v_cvt_pk_bf16_f32 v114, v114, v115
	v_cvt_pk_bf16_f32 v115, v120, v121
	global_store_dwordx4 v[124:125], v[112:115], off offset:256
	s_nop 1
	v_add_u32_e32 v112, s2, v140
	v_ashrrev_i32_e32 v113, 31, v112
	v_lshl_add_u64 v[114:115], v[112:113], 2, s[46:47]
	v_mov_b32_e32 v114, v153
	v_lshlrev_b64 v[112:113], 11, v[112:113]
	v_pk_mul_f32 v[108:109], v[108:109], v[114:115] op_sel_hi:[1,0]
	v_pk_mul_f32 v[116:117], v[106:107], v[114:115] op_sel_hi:[1,0]
	v_pk_mul_f32 v[106:107], v[104:105], v[114:115] op_sel_hi:[1,0]
	v_cvt_pk_bf16_f32 v104, v108, v109
	v_lshl_add_u64 v[108:109], s[44:45], 0, v[112:113]
	v_lshl_add_u64 v[108:109], v[108:109], 0, s[30:31]
	v_pk_mul_f32 v[110:111], v[110:111], v[114:115] op_sel_hi:[1,0]
	v_lshl_add_u64 v[108:109], v[108:109], 0, s[50:51]
	v_cvt_pk_bf16_f32 v105, v110, v111
	v_cvt_pk_bf16_f32 v106, v106, v107
	v_cvt_pk_bf16_f32 v107, v116, v117
	v_lshl_add_u64 v[108:109], v[108:109], 0, v[144:145]
	global_store_dwordx4 v[108:109], v[104:107], off
	v_pk_mul_f32 v[102:103], v[102:103], v[114:115] op_sel_hi:[1,0]
	v_pk_mul_f32 v[100:101], v[100:101], v[114:115] op_sel_hi:[1,0]
	v_pk_mul_f32 v[104:105], v[98:99], v[114:115] op_sel_hi:[1,0]
	v_pk_mul_f32 v[98:99], v[96:97], v[114:115] op_sel_hi:[1,0]
	v_cvt_pk_bf16_f32 v96, v100, v101
	v_cvt_pk_bf16_f32 v97, v102, v103
	v_cvt_pk_bf16_f32 v98, v98, v99
	v_cvt_pk_bf16_f32 v99, v104, v105
	global_store_dwordx4 v[108:109], v[96:99], off offset:256
	s_nop 1
	v_add_u32_e32 v96, s2, v141
	v_ashrrev_i32_e32 v97, 31, v96
	v_lshl_add_u64 v[98:99], v[96:97], 2, s[46:47]
	v_mov_b32_e32 v98, v154
	v_lshlrev_b64 v[96:97], 11, v[96:97]
	v_pk_mul_f32 v[92:93], v[92:93], v[98:99] op_sel_hi:[1,0]
	v_pk_mul_f32 v[100:101], v[90:91], v[98:99] op_sel_hi:[1,0]
	v_pk_mul_f32 v[90:91], v[88:89], v[98:99] op_sel_hi:[1,0]
	v_cvt_pk_bf16_f32 v88, v92, v93
	v_lshl_add_u64 v[92:93], s[44:45], 0, v[96:97]
	v_lshl_add_u64 v[92:93], v[92:93], 0, s[30:31]
	v_pk_mul_f32 v[94:95], v[94:95], v[98:99] op_sel_hi:[1,0]
	v_lshl_add_u64 v[92:93], v[92:93], 0, s[50:51]
	v_cvt_pk_bf16_f32 v89, v94, v95
	v_cvt_pk_bf16_f32 v90, v90, v91
	v_cvt_pk_bf16_f32 v91, v100, v101
	v_lshl_add_u64 v[92:93], v[92:93], 0, v[144:145]
	global_store_dwordx4 v[92:93], v[88:91], off
	v_pk_mul_f32 v[86:87], v[86:87], v[98:99] op_sel_hi:[1,0]
	v_pk_mul_f32 v[84:85], v[84:85], v[98:99] op_sel_hi:[1,0]
	v_pk_mul_f32 v[88:89], v[82:83], v[98:99] op_sel_hi:[1,0]
	v_pk_mul_f32 v[82:83], v[80:81], v[98:99] op_sel_hi:[1,0]
	v_cvt_pk_bf16_f32 v80, v84, v85
	v_cvt_pk_bf16_f32 v81, v86, v87
	v_cvt_pk_bf16_f32 v82, v82, v83
	v_cvt_pk_bf16_f32 v83, v88, v89
	global_store_dwordx4 v[92:93], v[80:83], off offset:256
	s_nop 1
	v_add_u32_e32 v80, s2, v142
	v_ashrrev_i32_e32 v81, 31, v80
	v_lshl_add_u64 v[82:83], v[80:81], 2, s[46:47]
	v_mov_b32_e32 v82, v155
	v_lshlrev_b64 v[80:81], 11, v[80:81]
	s_mov_b64 s[2:3], -1
	v_pk_mul_f32 v[76:77], v[76:77], v[82:83] op_sel_hi:[1,0]
	v_pk_mul_f32 v[84:85], v[74:75], v[82:83] op_sel_hi:[1,0]
; __device__ __forceinline__ u32x4 pack8(f32x4 a, f32x4 b) { u32x4 w; w.x = pk2(a[0], a[1]); w.y = pk2(a[2], a[3]); w.z = pk2(b[0], b[1]); w.w = pk2(b[2], b[3]); return w; }
;     __device__ __forceinline__ void operator()(const f32x4 (&acc)[2][2][4][2], const Unit& u, int wr, int wc, int fr, int fq) const {
;     ...
;         for (int ai = 0; ai < 2; ++ai)
; #pragma unroll
;             for (int m = 0; m < 4; ++m) {
;                 const int row = u.pm * 256 + ai * 128 + wr * 64 + m * 16 + fr; const float gt = gate[row];
; #pragma unroll
;                 for (int bj = 0; bj < 2; ++bj) *(u32x4*)(Y + (size_t)row * D + 256 * jn + 128 * bj + 32 * wc + 8 * fq) = pack8(acc[ai][bj][m][0] * gt, acc[ai][bj][m][1] * gt);
;             }
	v_pk_mul_f32 v[74:75], v[72:73], v[82:83] op_sel_hi:[1,0]
	v_cvt_pk_bf16_f32 v72, v76, v77
	v_lshl_add_u64 v[76:77], s[44:45], 0, v[80:81]
	v_lshl_add_u64 v[76:77], v[76:77], 0, s[30:31]
	v_pk_mul_f32 v[78:79], v[78:79], v[82:83] op_sel_hi:[1,0]
	v_lshl_add_u64 v[76:77], v[76:77], 0, s[50:51]
	v_cvt_pk_bf16_f32 v73, v78, v79
	v_cvt_pk_bf16_f32 v74, v74, v75
	v_cvt_pk_bf16_f32 v75, v84, v85
	v_lshl_add_u64 v[76:77], v[76:77], 0, v[144:145]
	global_store_dwordx4 v[76:77], v[72:75], off
	v_pk_mul_f32 v[70:71], v[70:71], v[82:83] op_sel_hi:[1,0]
	v_pk_mul_f32 v[68:69], v[68:69], v[82:83] op_sel_hi:[1,0]
	v_pk_mul_f32 v[72:73], v[66:67], v[82:83] op_sel_hi:[1,0]
	v_pk_mul_f32 v[66:67], v[64:65], v[82:83] op_sel_hi:[1,0]
	v_cvt_pk_bf16_f32 v64, v68, v69
	v_cvt_pk_bf16_f32 v65, v70, v71
	v_cvt_pk_bf16_f32 v66, v66, v67
	v_cvt_pk_bf16_f32 v67, v72, v73
	global_store_dwordx4 v[76:77], v[64:67], off offset:256
	s_nop 1
	v_add_u32_e32 v64, 0x80, v136
	v_ashrrev_i32_e32 v65, 31, v64
	v_lshl_add_u64 v[66:67], v[64:65], 2, s[46:47]
	v_mov_b32_e32 v66, v156
	v_lshlrev_b64 v[64:65], 11, v[64:65]
	v_pk_mul_f32 v[60:61], v[60:61], v[66:67] op_sel_hi:[1,0]
	v_pk_mul_f32 v[68:69], v[58:59], v[66:67] op_sel_hi:[1,0]
	v_pk_mul_f32 v[58:59], v[56:57], v[66:67] op_sel_hi:[1,0]
	v_cvt_pk_bf16_f32 v56, v60, v61
	v_lshl_add_u64 v[60:61], s[44:45], 0, v[64:65]
	v_lshl_add_u64 v[60:61], v[60:61], 0, s[30:31]
	v_pk_mul_f32 v[62:63], v[62:63], v[66:67] op_sel_hi:[1,0]
	v_lshl_add_u64 v[60:61], v[60:61], 0, s[50:51]
	v_cvt_pk_bf16_f32 v57, v62, v63
	v_cvt_pk_bf16_f32 v58, v58, v59
	v_cvt_pk_bf16_f32 v59, v68, v69
	v_lshl_add_u64 v[60:61], v[60:61], 0, v[144:145]
	global_store_dwordx4 v[60:61], v[56:59], off
	v_pk_mul_f32 v[54:55], v[54:55], v[66:67] op_sel_hi:[1,0]
	v_pk_mul_f32 v[52:53], v[52:53], v[66:67] op_sel_hi:[1,0]
	v_pk_mul_f32 v[56:57], v[50:51], v[66:67] op_sel_hi:[1,0]
	v_pk_mul_f32 v[50:51], v[48:49], v[66:67] op_sel_hi:[1,0]
	v_cvt_pk_bf16_f32 v48, v52, v53
	v_cvt_pk_bf16_f32 v49, v54, v55
	v_cvt_pk_bf16_f32 v50, v50, v51
	v_cvt_pk_bf16_f32 v51, v56, v57
	global_store_dwordx4 v[60:61], v[48:51], off offset:256
	s_nop 1
	v_add_u32_e32 v48, 0x90, v136
	v_ashrrev_i32_e32 v49, 31, v48
	v_lshl_add_u64 v[50:51], v[48:49], 2, s[46:47]
	v_mov_b32_e32 v50, v157
	v_lshlrev_b64 v[48:49], 11, v[48:49]
	v_pk_mul_f32 v[44:45], v[44:45], v[50:51] op_sel_hi:[1,0]
	v_pk_mul_f32 v[52:53], v[42:43], v[50:51] op_sel_hi:[1,0]
	v_pk_mul_f32 v[42:43], v[40:41], v[50:51] op_sel_hi:[1,0]
	v_cvt_pk_bf16_f32 v40, v44, v45
	v_lshl_add_u64 v[44:45], s[44:45], 0, v[48:49]
	v_lshl_add_u64 v[44:45], v[44:45], 0, s[30:31]
	v_pk_mul_f32 v[46:47], v[46:47], v[50:51] op_sel_hi:[1,0]
	v_lshl_add_u64 v[44:45], v[44:45], 0, s[50:51]
	v_cvt_pk_bf16_f32 v41, v46, v47
	v_cvt_pk_bf16_f32 v42, v42, v43
	v_cvt_pk_bf16_f32 v43, v52, v53
	v_lshl_add_u64 v[44:45], v[44:45], 0, v[144:145]
	global_store_dwordx4 v[44:45], v[40:43], off
	v_pk_mul_f32 v[38:39], v[38:39], v[50:51] op_sel_hi:[1,0]
	v_pk_mul_f32 v[36:37], v[36:37], v[50:51] op_sel_hi:[1,0]
	v_pk_mul_f32 v[40:41], v[34:35], v[50:51] op_sel_hi:[1,0]
	v_pk_mul_f32 v[34:35], v[32:33], v[50:51] op_sel_hi:[1,0]
	v_cvt_pk_bf16_f32 v32, v36, v37
	v_cvt_pk_bf16_f32 v33, v38, v39
	v_cvt_pk_bf16_f32 v34, v34, v35
	v_cvt_pk_bf16_f32 v35, v40, v41
	global_store_dwordx4 v[44:45], v[32:35], off offset:256
	s_nop 1
	v_add_u32_e32 v32, 0xa0, v136
	v_ashrrev_i32_e32 v33, 31, v32
	v_lshl_add_u64 v[34:35], v[32:33], 2, s[46:47]
	v_mov_b32_e32 v34, v158
	v_lshlrev_b64 v[32:33], 11, v[32:33]
	v_pk_mul_f32 v[28:29], v[28:29], v[34:35] op_sel_hi:[1,0]
	v_pk_mul_f32 v[36:37], v[26:27], v[34:35] op_sel_hi:[1,0]
	v_pk_mul_f32 v[26:27], v[24:25], v[34:35] op_sel_hi:[1,0]
	v_cvt_pk_bf16_f32 v24, v28, v29
	v_lshl_add_u64 v[28:29], s[44:45], 0, v[32:33]
	v_lshl_add_u64 v[28:29], v[28:29], 0, s[30:31]
	v_pk_mul_f32 v[30:31], v[30:31], v[34:35] op_sel_hi:[1,0]
	v_lshl_add_u64 v[28:29], v[28:29], 0, s[50:51]
	v_cvt_pk_bf16_f32 v25, v30, v31
	v_cvt_pk_bf16_f32 v26, v26, v27
	v_cvt_pk_bf16_f32 v27, v36, v37
	v_lshl_add_u64 v[28:29], v[28:29], 0, v[144:145]
	global_store_dwordx4 v[28:29], v[24:27], off
	v_pk_mul_f32 v[22:23], v[22:23], v[34:35] op_sel_hi:[1,0]
	v_pk_mul_f32 v[20:21], v[20:21], v[34:35] op_sel_hi:[1,0]
	v_pk_mul_f32 v[24:25], v[18:19], v[34:35] op_sel_hi:[1,0]
	v_pk_mul_f32 v[18:19], v[16:17], v[34:35] op_sel_hi:[1,0]
	v_cvt_pk_bf16_f32 v16, v20, v21
	v_cvt_pk_bf16_f32 v17, v22, v23
	v_cvt_pk_bf16_f32 v18, v18, v19
	v_cvt_pk_bf16_f32 v19, v24, v25
	global_store_dwordx4 v[28:29], v[16:19], off offset:256
	s_nop 1
	v_add_u32_e32 v16, 0xb0, v136
	v_ashrrev_i32_e32 v17, 31, v16
	v_lshl_add_u64 v[18:19], v[16:17], 2, s[46:47]
	v_mov_b32_e32 v18, v159
	v_lshlrev_b64 v[16:17], 11, v[16:17]
	v_pk_mul_f32 v[12:13], v[12:13], v[18:19] op_sel_hi:[1,0]
	v_pk_mul_f32 v[20:21], v[10:11], v[18:19] op_sel_hi:[1,0]
	v_pk_mul_f32 v[10:11], v[8:9], v[18:19] op_sel_hi:[1,0]
	v_cvt_pk_bf16_f32 v8, v12, v13
	v_lshl_add_u64 v[12:13], s[44:45], 0, v[16:17]
	v_lshl_add_u64 v[12:13], v[12:13], 0, s[30:31]
	v_pk_mul_f32 v[14:15], v[14:15], v[18:19] op_sel_hi:[1,0]
	v_lshl_add_u64 v[12:13], v[12:13], 0, s[50:51]
	v_cvt_pk_bf16_f32 v9, v14, v15
	v_cvt_pk_bf16_f32 v10, v10, v11
	v_cvt_pk_bf16_f32 v11, v20, v21
	v_lshl_add_u64 v[12:13], v[12:13], 0, v[144:145]
	global_store_dwordx4 v[12:13], v[8:11], off
	v_pk_mul_f32 v[6:7], v[6:7], v[18:19] op_sel_hi:[1,0]
	v_pk_mul_f32 v[4:5], v[4:5], v[18:19] op_sel_hi:[1,0]
	v_pk_mul_f32 v[8:9], v[2:3], v[18:19] op_sel_hi:[1,0]
	v_pk_mul_f32 v[2:3], v[0:1], v[18:19] op_sel_hi:[1,0]
	v_cvt_pk_bf16_f32 v0, v4, v5
	v_cvt_pk_bf16_f32 v1, v6, v7
	v_cvt_pk_bf16_f32 v2, v2, v3
	v_cvt_pk_bf16_f32 v3, v8, v9
	global_store_dwordx4 v[12:13], v[0:3], off offset:256
	s_cbranch_vccnz .LBB0_1274
	s_andn2_b64 vcc, exec, s[42:43]
	s_cbranch_vccnz .LBB0_1273
	s_barrier
	s_branch .LBB0_1273
